# attention input projection epilogue: head-norm cross-lane sums via permlane swaps instead of ds_bpermute (on top of the N1 reduction change)
# baseline (speedup 1.0000x reference)
; #define LAS __attribute__((address_space(3)))
;     ...
;         if constexpr (FP8) { asm volatile("s_nop 15\n\ts_nop 15\n\ts_nop 15\n\ts_nop 15" ::: "memory"); }
;     __device__ __forceinline__ void operator()(const f32x4 (&acc)[2][2][4][2], const Unit& u, int wr, int wc, int fr, int fq) const {
;         const int pn = u.pn, grp = pn >= 3 ? 1 : 0, pl = pn - 3 * grp;
;         const bool isq = pl < 2, isv = (pl == 2) && (wc >= 2), lat = u.pm < (NLAT / 256);
;         const float* gam = gam4 + (grp * 2 + (isq ? 0 : 1)) * 64;
;         f32x4 gv[2][2];
; #pragma unroll
;         for (int bj = 0; bj < 2; ++bj)
; #pragma unroll
;             for (int n = 0; n < 2; ++n) gv[bj][n] = *(const f32x4*)(gam + 32 * bj + 16 * n + 4 * fq);
;         const float qs = isq ? C2 : 1.f;
;         constexpr float ds = 1.0f / (SC_W * SC_H2);
;         constexpr float EPSA = EPS / (ds * ds);
; #pragma unroll
;         for (int ai = 0; ai < 2; ++ai)
; #pragma unroll
;             for (int m = 0; m < 4; ++m) {
;                 const int r = u.pm * BM + ai * HALF + wr * 64 + m * 16 + fr;
;                 f32x4 v[2][2];
;                 if (ai == 0 && m == 0) __builtin_amdgcn_s_waitcnt(0x0F70);
;                 if (!isv) {
;                     const f32x4 s4 = (acc[ai][0][m][0] * acc[ai][0][m][0] + acc[ai][0][m][1] * acc[ai][0][m][1]) + (acc[ai][1][m][0] * acc[ai][1][m][0] + acc[ai][1][m][1] * acc[ai][1][m][1]);
;                     float ss = (s4[0] + s4[1]) + (s4[2] + s4[3]);
;                     ss += __shfl_xor(ss, 16); ss += __shfl_xor(ss, 32);
;                     const float rs = __builtin_amdgcn_rsqf(ss * (1.0f / 64.0f) + EPSA) * qs;
; #pragma unroll
;                     for (int bj = 0; bj < 2; ++bj)
; #pragma unroll
;                         for (int n = 0; n < 2; ++n) v[bj][n] = acc[ai][bj][m][n] * (gv[bj][n] * rs);
;                     if (lat) {
; #pragma unroll
;                         for (int bj = 0; bj < 2; ++bj) { const int pos = bj ? (m * 16 + fr) : ((u.pm & 7) * 4 + ai * 2 + wr);
;                             const f32x4 cx = *(const LAS f32x4*)(ropeL + pos * 32 + 4 * fq), cy = *(const LAS f32x4*)(ropeL + pos * 32 + 16 + 4 * fq), a = v[bj][0], b = v[bj][1];
;                             v[bj][0] = a * cx - b * cy; v[bj][1] = a * cy + b * cx; }
.LBB0_673:
	s_cmp_gt_i32 s6, 2
	s_cselect_b64 s[28:29], -1, 0
	s_and_b64 s[8:9], s[28:29], exec
	s_cselect_b32 s3, -3, 0
	s_cselect_b32 s12, 2, 0
	s_add_i32 s3, s3, s6
	s_cmp_lt_i32 s3, 2
	s_cselect_b64 s[8:9], -1, 0
	s_cmp_gt_i32 s3, 1
	s_cselect_b64 s[30:31], -1, 0
	v_cndmask_b32_e64 v2, 0, 1, s[30:31]
	v_or_b32_e32 v2, s12, v2
	v_lshlrev_b32_e32 v190, 8, v2
	s_nop 15
	s_nop 15
	s_nop 15
	s_nop 15
	v_lshl_add_u64 v[2:3], v[168:169], 0, v[190:191]
	global_load_dwordx4 v[14:17], v[2:3], off
	global_load_dwordx4 v[10:13], v[2:3], off offset:64
	global_load_dwordx4 v[6:9], v[2:3], off offset:128
	s_nop 0
	global_load_dwordx4 v[2:5], v[2:3], off offset:192
	s_cmp_lg_u32 s3, 2
	s_cselect_b64 s[6:7], -1, 0
	s_or_b64 s[6:7], s[6:7], s[22:23]
	s_cmpk_lt_i32 s2, 0x80
	s_cselect_b64 s[38:39], -1, 0
	v_cndmask_b32_e64 v173, v213, 1.0, s[30:31]
	s_lshl_b32 s30, s2, 2
	s_and_b32 s30, s30, 28
	v_cndmask_b32_e64 v18, 0, 1, s[38:39]
	s_mov_b64 s[18:19], -1
	s_add_i32 s30, s30, s33
	s_and_b64 vcc, exec, s[6:7]
	v_cmp_ne_u32_e64 s[38:39], 1, v18
	s_waitcnt vmcnt(0)
	s_cbranch_vccz .LBB0_677
	v_pk_mul_f32 v[18:19], v[152:153], v[152:153]
	v_pk_mul_f32 v[20:21], v[150:151], v[150:151]
	v_pk_mul_f32 v[22:23], v[160:161], v[160:161]
	v_pk_mul_f32 v[24:25], v[158:159], v[158:159]
	v_pk_fma_f32 v[18:19], v[148:149], v[148:149], v[18:19]
	v_pk_fma_f32 v[20:21], v[146:147], v[146:147], v[20:21]
	v_pk_fma_f32 v[22:23], v[156:157], v[156:157], v[22:23]
	v_pk_fma_f32 v[24:25], v[154:155], v[154:155], v[24:25]
	v_pk_add_f32 v[18:19], v[18:19], v[22:23]
	v_pk_add_f32 v[20:21], v[20:21], v[24:25]
	s_nop 0
	v_pk_mov_b32 v[22:23], v[20:21], v[18:19] op_sel:[1,0]
	v_mov_b32_e32 v21, v19
	v_pk_add_f32 v[18:19], v[22:23], v[20:21]
	v_and_b32_e32 v20, 64, v211
	v_add_f32_e32 v18, v18, v19
	v_xor_b32_e32 v19, 16, v211
	v_add_u32_e32 v20, 64, v20
	v_cmp_lt_i32_e32 vcc, v19, v20
	s_nop 1
	v_cndmask_b32_e32 v19, v211, v19, vcc
	v_lshlrev_b32_e32 v19, 2, v19
	s_waitcnt lgkmcnt(0)
	v_mov_b32_e32 v19, v18
	s_nop 1
	v_permlane16_swap_b32_e32 v19, v18
	v_add_f32_e32 v18, v18, v19
	v_xor_b32_e32 v19, 32, v211
	v_cmp_lt_i32_e32 vcc, v19, v20
	s_nop 1
	v_cndmask_b32_e32 v19, v211, v19, vcc
	v_lshlrev_b32_e32 v19, 2, v19
	s_and_b64 vcc, exec, s[38:39]
	s_waitcnt lgkmcnt(0)
	v_mov_b32_e32 v19, v18
	s_nop 1
	v_permlane32_swap_b32_e32 v19, v18
	v_add_f32_e32 v18, v18, v19
	v_fmamk_f32 v18, v18, 0x3c800000, v210
	v_rsq_f32_e32 v18, v18
	s_nop 0
	v_mul_f32_e32 v26, v173, v18
	v_pk_mul_f32 v[18:19], v[14:15], v[26:27] op_sel_hi:[1,0]
	v_pk_mul_f32 v[20:21], v[16:17], v[26:27] op_sel_hi:[1,0]
	v_pk_mul_f32 v[30:31], v[146:147], v[18:19]
	v_pk_mul_f32 v[32:33], v[148:149], v[20:21]
	v_pk_mul_f32 v[18:19], v[10:11], v[26:27] op_sel_hi:[1,0]
	v_pk_mul_f32 v[20:21], v[12:13], v[26:27] op_sel_hi:[1,0]
	v_pk_mul_f32 v[22:23], v[6:7], v[26:27] op_sel_hi:[1,0]
	v_pk_mul_f32 v[24:25], v[8:9], v[26:27] op_sel_hi:[1,0]
	v_pk_mul_f32 v[174:175], v[2:3], v[26:27] op_sel_hi:[1,0]
	v_pk_mul_f32 v[26:27], v[4:5], v[26:27] op_sel_hi:[1,0]
	v_pk_mul_f32 v[20:21], v[152:153], v[20:21]
	v_pk_mul_f32 v[18:19], v[150:151], v[18:19]
	v_pk_mul_f32 v[24:25], v[156:157], v[24:25]
	v_pk_mul_f32 v[22:23], v[154:155], v[22:23]
	v_pk_mul_f32 v[28:29], v[160:161], v[26:27]
	v_pk_mul_f32 v[26:27], v[158:159], v[174:175]
	s_cbranch_vccnz .LBB0_676
	v_lshl_add_u32 v178, s30, 7, v170
	ds_read_b128 v[174:177], v178
	ds_read_b128 v[178:181], v178 offset:64
	s_waitcnt lgkmcnt(0)
	v_pk_mul_f32 v[182:183], v[20:21], v[180:181]
	v_pk_mul_f32 v[186:187], v[18:19], v[178:179]
	v_pk_fma_f32 v[184:185], v[32:33], v[176:177], v[182:183] neg_lo:[0,0,1] neg_hi:[0,0,1]
	v_pk_fma_f32 v[182:183], v[30:31], v[174:175], v[186:187] neg_lo:[0,0,1] neg_hi:[0,0,1]
	v_pk_mul_f32 v[32:33], v[32:33], v[180:181]
	v_pk_mul_f32 v[30:31], v[30:31], v[178:179]
	v_pk_fma_f32 v[20:21], v[20:21], v[176:177], v[32:33]
	v_pk_fma_f32 v[18:19], v[18:19], v[174:175], v[30:31]
	ds_read_b128 v[30:33], v171
	ds_read_b128 v[174:177], v171 offset:64
	s_waitcnt lgkmcnt(0)
	v_pk_mul_f32 v[178:179], v[28:29], v[176:177]
	v_pk_mul_f32 v[186:187], v[26:27], v[174:175]
	v_pk_fma_f32 v[180:181], v[24:25], v[32:33], v[178:179] neg_lo:[0,0,1] neg_hi:[0,0,1]
	v_pk_fma_f32 v[178:179], v[22:23], v[30:31], v[186:187] neg_lo:[0,0,1] neg_hi:[0,0,1]
	v_pk_mul_f32 v[24:25], v[24:25], v[176:177]
	v_pk_mul_f32 v[22:23], v[22:23], v[174:175]
	v_pk_fma_f32 v[28:29], v[28:29], v[32:33], v[24:25]
	v_pk_fma_f32 v[26:27], v[26:27], v[30:31], v[22:23]
	v_mov_b64_e32 v[30:31], v[182:183]
	v_mov_b64_e32 v[22:23], v[178:179]
	v_mov_b64_e32 v[32:33], v[184:185]
	v_mov_b64_e32 v[24:25], v[180:181]

; #define LAS __attribute__((address_space(3)))
; __device__ __forceinline__ unsigned cvt_pk_bf16(float lo, float hi) { unsigned r; asm volatile("v_cvt_pk_bf16_f32 %0, %1, %2" : "=v"(r) : "v"(lo), "v"(hi)); return r; }
;     __device__ __forceinline__ void operator()(const f32x4 (&acc)[2][2][4][2], const Unit& u, int wr, int wc, int fr, int fq) const {
;     ...
;                 if (!isv) {
;                     const f32x4 s4 = (acc[ai][0][m][0] * acc[ai][0][m][0] + acc[ai][0][m][1] * acc[ai][0][m][1]) + (acc[ai][1][m][0] * acc[ai][1][m][0] + acc[ai][1][m][1] * acc[ai][1][m][1]);
;                     float ss = (s4[0] + s4[1]) + (s4[2] + s4[3]);
;                     ss += __shfl_xor(ss, 16); ss += __shfl_xor(ss, 32);
;                     const float rs = __builtin_amdgcn_rsqf(ss * (1.0f / 64.0f) + EPSA) * qs;
; #pragma unroll
;                     for (int bj = 0; bj < 2; ++bj)
; #pragma unroll
;                         for (int n = 0; n < 2; ++n) v[bj][n] = acc[ai][bj][m][n] * (gv[bj][n] * rs);
;                     if (lat) {
; #pragma unroll
;                         for (int bj = 0; bj < 2; ++bj) { const int pos = bj ? (m * 16 + fr) : ((u.pm & 7) * 4 + ai * 2 + wr);
;                             const f32x4 cx = *(const LAS f32x4*)(ropeL + pos * 32 + 4 * fq), cy = *(const LAS f32x4*)(ropeL + pos * 32 + 16 + 4 * fq), a = v[bj][0], b = v[bj][1];
;                             v[bj][0] = a * cx - b * cy; v[bj][1] = a * cy + b * cx; }
;                     }
;                 } else {
; #pragma unroll
;                     for (int bj = 0; bj < 2; ++bj)
; #pragma unroll
;                         for (int n = 0; n < 2; ++n) v[bj][n] = acc[ai][bj][m][n] * ds;
;                 }
;                 bf16_t* dst;
;                 if (isq) dst = Q + (size_t)r * D + (grp * 8 + pl * 4 + wc) * HD;
;                 else if (!isv) dst = Kb + (size_t)kv_row(r) * KVP + (grp * 2 + wc) * HD;
;                 else dst = Vb + (size_t)kv_row(r) * KVP + (grp * 2 + wc - 2) * HD;
; #pragma unroll
;                 for (int bj = 0; bj < 2; ++bj)
; #pragma unroll
;                     for (int n = 0; n < 2; ++n) { u32x2 w; w.x = cvt_pk_bf16(v[bj][n][0], v[bj][n][1]); w.y = cvt_pk_bf16(v[bj][n][2], v[bj][n][3]);
;                         *(u32x2*)(dst + 32 * bj + 16 * n + 4 * fq) = w; }
.LBB0_686:
	v_lshlrev_b32_e32 v190, 1, v166
	v_lshl_add_u64 v[148:149], v[148:149], 0, v[190:191]
	v_cvt_pk_bf16_f32 v30, v30, v31
	v_cvt_pk_bf16_f32 v31, v32, v33
	global_store_dwordx2 v[148:149], v[30:31], off
	v_cvt_pk_bf16_f32 v18, v18, v19
	v_cvt_pk_bf16_f32 v19, v20, v21
	global_store_dwordx2 v[148:149], v[18:19], off offset:32
	v_cvt_pk_bf16_f32 v18, v22, v23
	v_cvt_pk_bf16_f32 v19, v24, v25
	global_store_dwordx2 v[148:149], v[18:19], off offset:64
	v_cvt_pk_bf16_f32 v18, v26, v27
	v_cvt_pk_bf16_f32 v19, v28, v29
	s_and_b64 vcc, exec, s[40:41]
	s_mov_b64 s[2:3], -1
	global_store_dwordx2 v[148:149], v[18:19], off offset:96
	s_cbranch_vccnz .LBB0_690
	v_pk_mul_f32 v[18:19], v[132:133], v[132:133]
	v_pk_mul_f32 v[20:21], v[130:131], v[130:131]
	v_pk_mul_f32 v[22:23], v[140:141], v[140:141]
	v_pk_mul_f32 v[24:25], v[138:139], v[138:139]
	v_pk_fma_f32 v[18:19], v[136:137], v[136:137], v[18:19]
	v_pk_fma_f32 v[20:21], v[134:135], v[134:135], v[20:21]
	v_pk_fma_f32 v[22:23], v[144:145], v[144:145], v[22:23]
	v_pk_fma_f32 v[24:25], v[142:143], v[142:143], v[24:25]
	v_pk_add_f32 v[18:19], v[18:19], v[22:23]
	v_pk_add_f32 v[20:21], v[20:21], v[24:25]
	s_nop 0
	v_pk_mov_b32 v[22:23], v[20:21], v[18:19] op_sel:[1,0]
	v_mov_b32_e32 v21, v19
	v_pk_add_f32 v[18:19], v[22:23], v[20:21]
	v_and_b32_e32 v20, 64, v211
	v_add_f32_e32 v18, v18, v19
	v_xor_b32_e32 v19, 16, v211
	v_add_u32_e32 v20, 64, v20
	v_cmp_lt_i32_e32 vcc, v19, v20
	s_nop 1
	v_cndmask_b32_e32 v19, v211, v19, vcc
	v_lshlrev_b32_e32 v19, 2, v19
	s_waitcnt lgkmcnt(0)
	v_mov_b32_e32 v19, v18
	s_nop 1
	v_permlane16_swap_b32_e32 v19, v18
	v_add_f32_e32 v18, v18, v19
	v_xor_b32_e32 v19, 32, v211
	v_cmp_lt_i32_e32 vcc, v19, v20
	s_nop 1
	v_cndmask_b32_e32 v19, v211, v19, vcc
	v_lshlrev_b32_e32 v19, 2, v19
	s_and_b64 vcc, exec, s[38:39]
	s_waitcnt lgkmcnt(0)
	v_mov_b32_e32 v19, v18
	s_nop 1
	v_permlane32_swap_b32_e32 v19, v18
	v_add_f32_e32 v18, v18, v19
	v_fmamk_f32 v18, v18, 0x3c800000, v210
	v_rsq_f32_e32 v18, v18
	s_nop 0
	v_mul_f32_e32 v26, v173, v18
	v_pk_mul_f32 v[18:19], v[14:15], v[26:27] op_sel_hi:[1,0]
	v_pk_mul_f32 v[20:21], v[16:17], v[26:27] op_sel_hi:[1,0]
	v_pk_mul_f32 v[30:31], v[134:135], v[18:19]
	v_pk_mul_f32 v[32:33], v[136:137], v[20:21]
	v_pk_mul_f32 v[18:19], v[10:11], v[26:27] op_sel_hi:[1,0]
	v_pk_mul_f32 v[20:21], v[12:13], v[26:27] op_sel_hi:[1,0]
	v_pk_mul_f32 v[22:23], v[6:7], v[26:27] op_sel_hi:[1,0]
	v_pk_mul_f32 v[24:25], v[8:9], v[26:27] op_sel_hi:[1,0]
	v_pk_mul_f32 v[148:149], v[2:3], v[26:27] op_sel_hi:[1,0]
	v_pk_mul_f32 v[26:27], v[4:5], v[26:27] op_sel_hi:[1,0]
	v_pk_mul_f32 v[20:21], v[132:133], v[20:21]
	v_pk_mul_f32 v[18:19], v[130:131], v[18:19]
	v_pk_mul_f32 v[24:25], v[144:145], v[24:25]
	v_pk_mul_f32 v[22:23], v[142:143], v[22:23]
	v_pk_mul_f32 v[28:29], v[140:141], v[26:27]
	v_pk_mul_f32 v[26:27], v[138:139], v[148:149]
	s_cbranch_vccnz .LBB0_689
	v_lshl_add_u32 v147, s30, 7, v170
	ds_read_b128 v[148:151], v147
	ds_read_b128 v[152:155], v147 offset:64
	s_waitcnt lgkmcnt(0)
	v_pk_mul_f32 v[156:157], v[20:21], v[154:155]
	v_pk_mul_f32 v[160:161], v[18:19], v[152:153]
	v_pk_fma_f32 v[158:159], v[32:33], v[150:151], v[156:157] neg_lo:[0,0,1] neg_hi:[0,0,1]
	v_pk_fma_f32 v[156:157], v[30:31], v[148:149], v[160:161] neg_lo:[0,0,1] neg_hi:[0,0,1]
	v_pk_mul_f32 v[32:33], v[32:33], v[154:155]
	v_pk_mul_f32 v[30:31], v[30:31], v[152:153]
	v_pk_fma_f32 v[20:21], v[20:21], v[150:151], v[32:33]
	v_pk_fma_f32 v[18:19], v[18:19], v[148:149], v[30:31]
	ds_read_b128 v[30:33], v171 offset:2048
	ds_read_b128 v[148:151], v171 offset:2112
	s_waitcnt lgkmcnt(0)
	v_pk_mul_f32 v[152:153], v[28:29], v[150:151]
	v_pk_mul_f32 v[160:161], v[26:27], v[148:149]
	v_pk_fma_f32 v[154:155], v[24:25], v[32:33], v[152:153] neg_lo:[0,0,1] neg_hi:[0,0,1]
	v_pk_fma_f32 v[152:153], v[22:23], v[30:31], v[160:161] neg_lo:[0,0,1] neg_hi:[0,0,1]
	v_pk_mul_f32 v[24:25], v[24:25], v[150:151]
	v_pk_mul_f32 v[22:23], v[22:23], v[148:149]
	v_pk_fma_f32 v[28:29], v[28:29], v[32:33], v[24:25]
	v_pk_fma_f32 v[26:27], v[26:27], v[30:31], v[22:23]
	v_mov_b64_e32 v[30:31], v[156:157]
	v_mov_b64_e32 v[22:23], v[152:153]
	v_mov_b64_e32 v[32:33], v[158:159]
	v_mov_b64_e32 v[24:25], v[154:155]

; #define LAS __attribute__((address_space(3)))
; __device__ __forceinline__ unsigned cvt_pk_bf16(float lo, float hi) { unsigned r; asm volatile("v_cvt_pk_bf16_f32 %0, %1, %2" : "=v"(r) : "v"(lo), "v"(hi)); return r; }
;     __device__ __forceinline__ void operator()(const f32x4 (&acc)[2][2][4][2], const Unit& u, int wr, int wc, int fr, int fq) const {
;     ...
;                 if (!isv) {
;                     const f32x4 s4 = (acc[ai][0][m][0] * acc[ai][0][m][0] + acc[ai][0][m][1] * acc[ai][0][m][1]) + (acc[ai][1][m][0] * acc[ai][1][m][0] + acc[ai][1][m][1] * acc[ai][1][m][1]);
;                     float ss = (s4[0] + s4[1]) + (s4[2] + s4[3]);
;                     ss += __shfl_xor(ss, 16); ss += __shfl_xor(ss, 32);
;                     const float rs = __builtin_amdgcn_rsqf(ss * (1.0f / 64.0f) + EPSA) * qs;
; #pragma unroll
;                     for (int bj = 0; bj < 2; ++bj)
; #pragma unroll
;                         for (int n = 0; n < 2; ++n) v[bj][n] = acc[ai][bj][m][n] * (gv[bj][n] * rs);
;                     if (lat) {
; #pragma unroll
;                         for (int bj = 0; bj < 2; ++bj) { const int pos = bj ? (m * 16 + fr) : ((u.pm & 7) * 4 + ai * 2 + wr);
;                             const f32x4 cx = *(const LAS f32x4*)(ropeL + pos * 32 + 4 * fq), cy = *(const LAS f32x4*)(ropeL + pos * 32 + 16 + 4 * fq), a = v[bj][0], b = v[bj][1];
;                             v[bj][0] = a * cx - b * cy; v[bj][1] = a * cy + b * cx; }
;                     }
;                 } else {
; #pragma unroll
;                     for (int bj = 0; bj < 2; ++bj)
; #pragma unroll
;                         for (int n = 0; n < 2; ++n) v[bj][n] = acc[ai][bj][m][n] * ds;
;                 }
;                 bf16_t* dst;
;                 if (isq) dst = Q + (size_t)r * D + (grp * 8 + pl * 4 + wc) * HD;
;                 else if (!isv) dst = Kb + (size_t)kv_row(r) * KVP + (grp * 2 + wc) * HD;
;                 else dst = Vb + (size_t)kv_row(r) * KVP + (grp * 2 + wc - 2) * HD;
; #pragma unroll
;                 for (int bj = 0; bj < 2; ++bj)
; #pragma unroll
;                     for (int n = 0; n < 2; ++n) { u32x2 w; w.x = cvt_pk_bf16(v[bj][n][0], v[bj][n][1]); w.y = cvt_pk_bf16(v[bj][n][2], v[bj][n][3]);
;                         *(u32x2*)(dst + 32 * bj + 16 * n + 4 * fq) = w; }
.LBB0_699:
	v_lshl_add_u64 v[130:131], v[130:131], 0, v[190:191]
	v_cvt_pk_bf16_f32 v30, v30, v31
	v_cvt_pk_bf16_f32 v31, v32, v33
	global_store_dwordx2 v[130:131], v[30:31], off
	v_cvt_pk_bf16_f32 v18, v18, v19
	v_cvt_pk_bf16_f32 v19, v20, v21
	global_store_dwordx2 v[130:131], v[18:19], off offset:32
	v_cvt_pk_bf16_f32 v18, v22, v23
	v_cvt_pk_bf16_f32 v19, v24, v25
	global_store_dwordx2 v[130:131], v[18:19], off offset:64
	v_cvt_pk_bf16_f32 v18, v26, v27
	v_cvt_pk_bf16_f32 v19, v28, v29
	s_and_b64 vcc, exec, s[40:41]
	s_mov_b64 s[2:3], -1
	global_store_dwordx2 v[130:131], v[18:19], off offset:96
	s_cbranch_vccnz .LBB0_703
	v_pk_mul_f32 v[18:19], v[116:117], v[116:117]
	v_pk_mul_f32 v[20:21], v[114:115], v[114:115]
	v_pk_mul_f32 v[22:23], v[124:125], v[124:125]
	v_pk_mul_f32 v[24:25], v[122:123], v[122:123]
	v_pk_fma_f32 v[18:19], v[120:121], v[120:121], v[18:19]
	v_pk_fma_f32 v[20:21], v[118:119], v[118:119], v[20:21]
	v_pk_fma_f32 v[22:23], v[128:129], v[128:129], v[22:23]
	v_pk_fma_f32 v[24:25], v[126:127], v[126:127], v[24:25]
	v_pk_add_f32 v[18:19], v[18:19], v[22:23]
	v_pk_add_f32 v[20:21], v[20:21], v[24:25]
	s_nop 0
	v_pk_mov_b32 v[22:23], v[20:21], v[18:19] op_sel:[1,0]
	v_mov_b32_e32 v21, v19
	v_pk_add_f32 v[18:19], v[22:23], v[20:21]
	v_and_b32_e32 v20, 64, v211
	v_add_f32_e32 v18, v18, v19
	v_xor_b32_e32 v19, 16, v211
	v_add_u32_e32 v20, 64, v20
	v_cmp_lt_i32_e32 vcc, v19, v20
	s_nop 1
	v_cndmask_b32_e32 v19, v211, v19, vcc
	v_lshlrev_b32_e32 v19, 2, v19
	s_waitcnt lgkmcnt(0)
	v_mov_b32_e32 v19, v18
	s_nop 1
	v_permlane16_swap_b32_e32 v19, v18
	v_add_f32_e32 v18, v18, v19
	v_xor_b32_e32 v19, 32, v211
	v_cmp_lt_i32_e32 vcc, v19, v20
	s_nop 1
	v_cndmask_b32_e32 v19, v211, v19, vcc
	v_lshlrev_b32_e32 v19, 2, v19
	s_and_b64 vcc, exec, s[38:39]
	s_waitcnt lgkmcnt(0)
	v_mov_b32_e32 v19, v18
	s_nop 1
	v_permlane32_swap_b32_e32 v19, v18
	v_add_f32_e32 v18, v18, v19
	v_fmamk_f32 v18, v18, 0x3c800000, v210
	v_rsq_f32_e32 v18, v18
	s_nop 0
	v_mul_f32_e32 v26, v173, v18
	v_pk_mul_f32 v[18:19], v[14:15], v[26:27] op_sel_hi:[1,0]
	v_pk_mul_f32 v[20:21], v[16:17], v[26:27] op_sel_hi:[1,0]
	v_pk_mul_f32 v[30:31], v[118:119], v[18:19]
	v_pk_mul_f32 v[32:33], v[120:121], v[20:21]
	v_pk_mul_f32 v[18:19], v[10:11], v[26:27] op_sel_hi:[1,0]
	v_pk_mul_f32 v[20:21], v[12:13], v[26:27] op_sel_hi:[1,0]
	v_pk_mul_f32 v[22:23], v[6:7], v[26:27] op_sel_hi:[1,0]
	v_pk_mul_f32 v[24:25], v[8:9], v[26:27] op_sel_hi:[1,0]
	v_pk_mul_f32 v[130:131], v[2:3], v[26:27] op_sel_hi:[1,0]
	v_pk_mul_f32 v[26:27], v[4:5], v[26:27] op_sel_hi:[1,0]
	v_pk_mul_f32 v[20:21], v[116:117], v[20:21]
	v_pk_mul_f32 v[18:19], v[114:115], v[18:19]
	v_pk_mul_f32 v[24:25], v[128:129], v[24:25]
	v_pk_mul_f32 v[22:23], v[126:127], v[22:23]
	v_pk_mul_f32 v[28:29], v[124:125], v[26:27]
	v_pk_mul_f32 v[26:27], v[122:123], v[130:131]
	s_cbranch_vccnz .LBB0_702
	v_lshl_add_u32 v134, s30, 7, v170
	ds_read_b128 v[130:133], v134
	ds_read_b128 v[134:137], v134 offset:64
	s_waitcnt lgkmcnt(0)
	v_pk_mul_f32 v[138:139], v[20:21], v[136:137]
	v_pk_mul_f32 v[142:143], v[18:19], v[134:135]
	v_pk_fma_f32 v[140:141], v[32:33], v[132:133], v[138:139] neg_lo:[0,0,1] neg_hi:[0,0,1]
	v_pk_fma_f32 v[138:139], v[30:31], v[130:131], v[142:143] neg_lo:[0,0,1] neg_hi:[0,0,1]
	v_pk_mul_f32 v[32:33], v[32:33], v[136:137]
	v_pk_mul_f32 v[30:31], v[30:31], v[134:135]
	v_pk_fma_f32 v[20:21], v[20:21], v[132:133], v[32:33]
	v_pk_fma_f32 v[18:19], v[18:19], v[130:131], v[30:31]
	ds_read_b128 v[30:33], v171 offset:4096
	ds_read_b128 v[130:133], v171 offset:4160
	s_waitcnt lgkmcnt(0)
	v_pk_mul_f32 v[134:135], v[28:29], v[132:133]
	v_pk_mul_f32 v[142:143], v[26:27], v[130:131]
	v_pk_fma_f32 v[136:137], v[24:25], v[32:33], v[134:135] neg_lo:[0,0,1] neg_hi:[0,0,1]
	v_pk_fma_f32 v[134:135], v[22:23], v[30:31], v[142:143] neg_lo:[0,0,1] neg_hi:[0,0,1]
	v_pk_mul_f32 v[24:25], v[24:25], v[132:133]
	v_pk_mul_f32 v[22:23], v[22:23], v[130:131]
	v_pk_fma_f32 v[28:29], v[28:29], v[32:33], v[24:25]
	v_pk_fma_f32 v[26:27], v[26:27], v[30:31], v[22:23]
	v_mov_b64_e32 v[30:31], v[138:139]
	v_mov_b64_e32 v[22:23], v[134:135]
	v_mov_b64_e32 v[32:33], v[140:141]
	v_mov_b64_e32 v[24:25], v[136:137]

; #define LAS __attribute__((address_space(3)))
; __device__ __forceinline__ unsigned cvt_pk_bf16(float lo, float hi) { unsigned r; asm volatile("v_cvt_pk_bf16_f32 %0, %1, %2" : "=v"(r) : "v"(lo), "v"(hi)); return r; }
;     __device__ __forceinline__ void operator()(const f32x4 (&acc)[2][2][4][2], const Unit& u, int wr, int wc, int fr, int fq) const {
;     ...
;                 if (!isv) {
;                     const f32x4 s4 = (acc[ai][0][m][0] * acc[ai][0][m][0] + acc[ai][0][m][1] * acc[ai][0][m][1]) + (acc[ai][1][m][0] * acc[ai][1][m][0] + acc[ai][1][m][1] * acc[ai][1][m][1]);
;                     float ss = (s4[0] + s4[1]) + (s4[2] + s4[3]);
;                     ss += __shfl_xor(ss, 16); ss += __shfl_xor(ss, 32);
;                     const float rs = __builtin_amdgcn_rsqf(ss * (1.0f / 64.0f) + EPSA) * qs;
; #pragma unroll
;                     for (int bj = 0; bj < 2; ++bj)
; #pragma unroll
;                         for (int n = 0; n < 2; ++n) v[bj][n] = acc[ai][bj][m][n] * (gv[bj][n] * rs);
;                     if (lat) {
; #pragma unroll
;                         for (int bj = 0; bj < 2; ++bj) { const int pos = bj ? (m * 16 + fr) : ((u.pm & 7) * 4 + ai * 2 + wr);
;                             const f32x4 cx = *(const LAS f32x4*)(ropeL + pos * 32 + 4 * fq), cy = *(const LAS f32x4*)(ropeL + pos * 32 + 16 + 4 * fq), a = v[bj][0], b = v[bj][1];
;                             v[bj][0] = a * cx - b * cy; v[bj][1] = a * cy + b * cx; }
;                     }
;                 } else {
; #pragma unroll
;                     for (int bj = 0; bj < 2; ++bj)
; #pragma unroll
;                         for (int n = 0; n < 2; ++n) v[bj][n] = acc[ai][bj][m][n] * ds;
;                 }
;                 bf16_t* dst;
;                 if (isq) dst = Q + (size_t)r * D + (grp * 8 + pl * 4 + wc) * HD;
;                 else if (!isv) dst = Kb + (size_t)kv_row(r) * KVP + (grp * 2 + wc) * HD;
;                 else dst = Vb + (size_t)kv_row(r) * KVP + (grp * 2 + wc - 2) * HD;
; #pragma unroll
;                 for (int bj = 0; bj < 2; ++bj)
; #pragma unroll
;                     for (int n = 0; n < 2; ++n) { u32x2 w; w.x = cvt_pk_bf16(v[bj][n][0], v[bj][n][1]); w.y = cvt_pk_bf16(v[bj][n][2], v[bj][n][3]);
;                         *(u32x2*)(dst + 32 * bj + 16 * n + 4 * fq) = w; }
.LBB0_712:
	v_lshl_add_u64 v[114:115], v[114:115], 0, v[190:191]
	v_cvt_pk_bf16_f32 v30, v30, v31
	v_cvt_pk_bf16_f32 v31, v32, v33
	global_store_dwordx2 v[114:115], v[30:31], off
	v_cvt_pk_bf16_f32 v18, v18, v19
	v_cvt_pk_bf16_f32 v19, v20, v21
	global_store_dwordx2 v[114:115], v[18:19], off offset:32
	v_cvt_pk_bf16_f32 v18, v22, v23
	v_cvt_pk_bf16_f32 v19, v24, v25
	global_store_dwordx2 v[114:115], v[18:19], off offset:64
	v_cvt_pk_bf16_f32 v18, v26, v27
	v_cvt_pk_bf16_f32 v19, v28, v29
	s_and_b64 vcc, exec, s[40:41]
	s_mov_b64 s[2:3], -1
	global_store_dwordx2 v[114:115], v[18:19], off offset:96
	s_cbranch_vccnz .LBB0_716
	v_pk_mul_f32 v[18:19], v[100:101], v[100:101]
	v_pk_mul_f32 v[20:21], v[98:99], v[98:99]
	v_pk_mul_f32 v[22:23], v[108:109], v[108:109]
	v_pk_mul_f32 v[24:25], v[106:107], v[106:107]
	v_pk_fma_f32 v[18:19], v[104:105], v[104:105], v[18:19]
	v_pk_fma_f32 v[20:21], v[102:103], v[102:103], v[20:21]
	v_pk_fma_f32 v[22:23], v[112:113], v[112:113], v[22:23]
	v_pk_fma_f32 v[24:25], v[110:111], v[110:111], v[24:25]
	v_pk_add_f32 v[18:19], v[18:19], v[22:23]
	v_pk_add_f32 v[20:21], v[20:21], v[24:25]
	s_nop 0
	v_pk_mov_b32 v[22:23], v[20:21], v[18:19] op_sel:[1,0]
	v_mov_b32_e32 v21, v19
	v_pk_add_f32 v[18:19], v[22:23], v[20:21]
	v_and_b32_e32 v20, 64, v211
	v_add_f32_e32 v18, v18, v19
	v_xor_b32_e32 v19, 16, v211
	v_add_u32_e32 v20, 64, v20
	v_cmp_lt_i32_e32 vcc, v19, v20
	s_nop 1
	v_cndmask_b32_e32 v19, v211, v19, vcc
	v_lshlrev_b32_e32 v19, 2, v19
	s_waitcnt lgkmcnt(0)
	v_mov_b32_e32 v19, v18
	s_nop 1
	v_permlane16_swap_b32_e32 v19, v18
	v_add_f32_e32 v18, v18, v19
	v_xor_b32_e32 v19, 32, v211
	v_cmp_lt_i32_e32 vcc, v19, v20
	s_nop 1
	v_cndmask_b32_e32 v19, v211, v19, vcc
	v_lshlrev_b32_e32 v19, 2, v19
	s_and_b64 vcc, exec, s[38:39]
	s_waitcnt lgkmcnt(0)
	v_mov_b32_e32 v19, v18
	s_nop 1
	v_permlane32_swap_b32_e32 v19, v18
	v_add_f32_e32 v18, v18, v19
	v_fmamk_f32 v18, v18, 0x3c800000, v210
	v_rsq_f32_e32 v18, v18
	s_nop 0
	v_mul_f32_e32 v26, v173, v18
	v_pk_mul_f32 v[18:19], v[14:15], v[26:27] op_sel_hi:[1,0]
	v_pk_mul_f32 v[20:21], v[16:17], v[26:27] op_sel_hi:[1,0]
	v_pk_mul_f32 v[30:31], v[102:103], v[18:19]
	v_pk_mul_f32 v[32:33], v[104:105], v[20:21]
	v_pk_mul_f32 v[18:19], v[10:11], v[26:27] op_sel_hi:[1,0]
	v_pk_mul_f32 v[20:21], v[12:13], v[26:27] op_sel_hi:[1,0]
	v_pk_mul_f32 v[22:23], v[6:7], v[26:27] op_sel_hi:[1,0]
	v_pk_mul_f32 v[24:25], v[8:9], v[26:27] op_sel_hi:[1,0]
	v_pk_mul_f32 v[114:115], v[2:3], v[26:27] op_sel_hi:[1,0]
	v_pk_mul_f32 v[26:27], v[4:5], v[26:27] op_sel_hi:[1,0]
	v_pk_mul_f32 v[20:21], v[100:101], v[20:21]
	v_pk_mul_f32 v[18:19], v[98:99], v[18:19]
	v_pk_mul_f32 v[24:25], v[112:113], v[24:25]
	v_pk_mul_f32 v[22:23], v[110:111], v[22:23]
	v_pk_mul_f32 v[28:29], v[108:109], v[26:27]
	v_pk_mul_f32 v[26:27], v[106:107], v[114:115]
	s_cbranch_vccnz .LBB0_715
	v_lshl_add_u32 v118, s30, 7, v170
	ds_read_b128 v[114:117], v118
	ds_read_b128 v[118:121], v118 offset:64
	s_waitcnt lgkmcnt(0)
	v_pk_mul_f32 v[122:123], v[20:21], v[120:121]
	v_pk_mul_f32 v[126:127], v[18:19], v[118:119]
	v_pk_fma_f32 v[124:125], v[32:33], v[116:117], v[122:123] neg_lo:[0,0,1] neg_hi:[0,0,1]
	v_pk_fma_f32 v[122:123], v[30:31], v[114:115], v[126:127] neg_lo:[0,0,1] neg_hi:[0,0,1]
	v_pk_mul_f32 v[32:33], v[32:33], v[120:121]
	v_pk_mul_f32 v[30:31], v[30:31], v[118:119]
	v_pk_fma_f32 v[20:21], v[20:21], v[116:117], v[32:33]
	v_pk_fma_f32 v[18:19], v[18:19], v[114:115], v[30:31]
	ds_read_b128 v[30:33], v171 offset:6144
	ds_read_b128 v[114:117], v171 offset:6208
	s_waitcnt lgkmcnt(0)
	v_pk_mul_f32 v[118:119], v[28:29], v[116:117]
	v_pk_mul_f32 v[126:127], v[26:27], v[114:115]
	v_pk_fma_f32 v[120:121], v[24:25], v[32:33], v[118:119] neg_lo:[0,0,1] neg_hi:[0,0,1]
	v_pk_fma_f32 v[118:119], v[22:23], v[30:31], v[126:127] neg_lo:[0,0,1] neg_hi:[0,0,1]
	v_pk_mul_f32 v[24:25], v[24:25], v[116:117]
	v_pk_mul_f32 v[22:23], v[22:23], v[114:115]
	v_pk_fma_f32 v[28:29], v[28:29], v[32:33], v[24:25]
	v_pk_fma_f32 v[26:27], v[26:27], v[30:31], v[22:23]
	v_mov_b64_e32 v[30:31], v[122:123]
	v_mov_b64_e32 v[22:23], v[118:119]
	v_mov_b64_e32 v[32:33], v[124:125]
	v_mov_b64_e32 v[24:25], v[120:121]

; #define LAS __attribute__((address_space(3)))
; __device__ __forceinline__ unsigned cvt_pk_bf16(float lo, float hi) { unsigned r; asm volatile("v_cvt_pk_bf16_f32 %0, %1, %2" : "=v"(r) : "v"(lo), "v"(hi)); return r; }
;     __device__ __forceinline__ void operator()(const f32x4 (&acc)[2][2][4][2], const Unit& u, int wr, int wc, int fr, int fq) const {
;     ...
;                 if (!isv) {
;                     const f32x4 s4 = (acc[ai][0][m][0] * acc[ai][0][m][0] + acc[ai][0][m][1] * acc[ai][0][m][1]) + (acc[ai][1][m][0] * acc[ai][1][m][0] + acc[ai][1][m][1] * acc[ai][1][m][1]);
;                     float ss = (s4[0] + s4[1]) + (s4[2] + s4[3]);
;                     ss += __shfl_xor(ss, 16); ss += __shfl_xor(ss, 32);
;                     const float rs = __builtin_amdgcn_rsqf(ss * (1.0f / 64.0f) + EPSA) * qs;
; #pragma unroll
;                     for (int bj = 0; bj < 2; ++bj)
; #pragma unroll
;                         for (int n = 0; n < 2; ++n) v[bj][n] = acc[ai][bj][m][n] * (gv[bj][n] * rs);
;                     if (lat) {
; #pragma unroll
;                         for (int bj = 0; bj < 2; ++bj) { const int pos = bj ? (m * 16 + fr) : ((u.pm & 7) * 4 + ai * 2 + wr);
;                             const f32x4 cx = *(const LAS f32x4*)(ropeL + pos * 32 + 4 * fq), cy = *(const LAS f32x4*)(ropeL + pos * 32 + 16 + 4 * fq), a = v[bj][0], b = v[bj][1];
;                             v[bj][0] = a * cx - b * cy; v[bj][1] = a * cy + b * cx; }
;                     }
;                 } else {
; #pragma unroll
;                     for (int bj = 0; bj < 2; ++bj)
; #pragma unroll
;                         for (int n = 0; n < 2; ++n) v[bj][n] = acc[ai][bj][m][n] * ds;
;                 }
;                 bf16_t* dst;
;                 if (isq) dst = Q + (size_t)r * D + (grp * 8 + pl * 4 + wc) * HD;
;                 else if (!isv) dst = Kb + (size_t)kv_row(r) * KVP + (grp * 2 + wc) * HD;
;                 else dst = Vb + (size_t)kv_row(r) * KVP + (grp * 2 + wc - 2) * HD;
; #pragma unroll
;                 for (int bj = 0; bj < 2; ++bj)
; #pragma unroll
;                     for (int n = 0; n < 2; ++n) { u32x2 w; w.x = cvt_pk_bf16(v[bj][n][0], v[bj][n][1]); w.y = cvt_pk_bf16(v[bj][n][2], v[bj][n][3]);
;                         *(u32x2*)(dst + 32 * bj + 16 * n + 4 * fq) = w; }
.LBB0_725:
	v_lshl_add_u64 v[98:99], v[98:99], 0, v[190:191]
	v_cvt_pk_bf16_f32 v30, v30, v31
	v_cvt_pk_bf16_f32 v31, v32, v33
	global_store_dwordx2 v[98:99], v[30:31], off
	v_cvt_pk_bf16_f32 v18, v18, v19
	v_cvt_pk_bf16_f32 v19, v20, v21
	global_store_dwordx2 v[98:99], v[18:19], off offset:32
	v_cvt_pk_bf16_f32 v18, v22, v23
	v_cvt_pk_bf16_f32 v19, v24, v25
	global_store_dwordx2 v[98:99], v[18:19], off offset:64
	v_cvt_pk_bf16_f32 v18, v26, v27
	v_cvt_pk_bf16_f32 v19, v28, v29
	s_add_i32 s30, s30, 2
	s_and_b64 vcc, exec, s[40:41]
	s_mov_b64 s[2:3], -1
	global_store_dwordx2 v[98:99], v[18:19], off offset:96
	s_cbranch_vccnz .LBB0_729
	v_pk_mul_f32 v[18:19], v[84:85], v[84:85]
	v_pk_mul_f32 v[20:21], v[82:83], v[82:83]
	v_pk_mul_f32 v[22:23], v[92:93], v[92:93]
	v_pk_mul_f32 v[24:25], v[90:91], v[90:91]
	v_pk_fma_f32 v[18:19], v[88:89], v[88:89], v[18:19]
	v_pk_fma_f32 v[20:21], v[86:87], v[86:87], v[20:21]
	v_pk_fma_f32 v[22:23], v[96:97], v[96:97], v[22:23]
	v_pk_fma_f32 v[24:25], v[94:95], v[94:95], v[24:25]
	v_pk_add_f32 v[18:19], v[18:19], v[22:23]
	v_pk_add_f32 v[20:21], v[20:21], v[24:25]
	s_nop 0
	v_pk_mov_b32 v[22:23], v[20:21], v[18:19] op_sel:[1,0]
	v_mov_b32_e32 v21, v19
	v_pk_add_f32 v[18:19], v[22:23], v[20:21]
	v_and_b32_e32 v20, 64, v211
	v_add_f32_e32 v18, v18, v19
	v_xor_b32_e32 v19, 16, v211
	v_add_u32_e32 v20, 64, v20
	v_cmp_lt_i32_e32 vcc, v19, v20
	s_nop 1
	v_cndmask_b32_e32 v19, v211, v19, vcc
	v_lshlrev_b32_e32 v19, 2, v19
	s_waitcnt lgkmcnt(0)
	v_mov_b32_e32 v19, v18
	s_nop 1
	v_permlane16_swap_b32_e32 v19, v18
	v_add_f32_e32 v18, v18, v19
	v_xor_b32_e32 v19, 32, v211
	v_cmp_lt_i32_e32 vcc, v19, v20
	s_nop 1
	v_cndmask_b32_e32 v19, v211, v19, vcc
	v_lshlrev_b32_e32 v19, 2, v19
	s_and_b64 vcc, exec, s[38:39]
	s_waitcnt lgkmcnt(0)
	v_mov_b32_e32 v19, v18
	s_nop 1
	v_permlane32_swap_b32_e32 v19, v18
	v_add_f32_e32 v18, v18, v19
	v_fmamk_f32 v18, v18, 0x3c800000, v210
	v_rsq_f32_e32 v18, v18
	s_nop 0
	v_mul_f32_e32 v26, v173, v18
	v_pk_mul_f32 v[18:19], v[14:15], v[26:27] op_sel_hi:[1,0]
	v_pk_mul_f32 v[20:21], v[16:17], v[26:27] op_sel_hi:[1,0]
	v_pk_mul_f32 v[30:31], v[86:87], v[18:19]
	v_pk_mul_f32 v[32:33], v[88:89], v[20:21]
	v_pk_mul_f32 v[18:19], v[10:11], v[26:27] op_sel_hi:[1,0]
	v_pk_mul_f32 v[20:21], v[12:13], v[26:27] op_sel_hi:[1,0]
	v_pk_mul_f32 v[22:23], v[6:7], v[26:27] op_sel_hi:[1,0]
	v_pk_mul_f32 v[24:25], v[8:9], v[26:27] op_sel_hi:[1,0]
	v_pk_mul_f32 v[98:99], v[2:3], v[26:27] op_sel_hi:[1,0]
	v_pk_mul_f32 v[26:27], v[4:5], v[26:27] op_sel_hi:[1,0]
	v_pk_mul_f32 v[20:21], v[84:85], v[20:21]
	v_pk_mul_f32 v[18:19], v[82:83], v[18:19]
	v_pk_mul_f32 v[24:25], v[96:97], v[24:25]
	v_pk_mul_f32 v[22:23], v[94:95], v[22:23]
	v_pk_mul_f32 v[28:29], v[92:93], v[26:27]
	v_pk_mul_f32 v[26:27], v[90:91], v[98:99]
	s_cbranch_vccnz .LBB0_728
	v_lshl_add_u32 v102, s30, 7, v170
	ds_read_b128 v[98:101], v102
	ds_read_b128 v[102:105], v102 offset:64
	s_waitcnt lgkmcnt(0)
	v_pk_mul_f32 v[106:107], v[20:21], v[104:105]
	v_pk_mul_f32 v[110:111], v[18:19], v[102:103]
	v_pk_fma_f32 v[108:109], v[32:33], v[100:101], v[106:107] neg_lo:[0,0,1] neg_hi:[0,0,1]
	v_pk_fma_f32 v[106:107], v[30:31], v[98:99], v[110:111] neg_lo:[0,0,1] neg_hi:[0,0,1]
	v_pk_mul_f32 v[32:33], v[32:33], v[104:105]
	v_pk_mul_f32 v[30:31], v[30:31], v[102:103]
	v_pk_fma_f32 v[20:21], v[20:21], v[100:101], v[32:33]
	v_pk_fma_f32 v[18:19], v[18:19], v[98:99], v[30:31]
	ds_read_b128 v[30:33], v171
	ds_read_b128 v[98:101], v171 offset:64
	s_waitcnt lgkmcnt(0)
	v_pk_mul_f32 v[102:103], v[28:29], v[100:101]
	v_pk_mul_f32 v[110:111], v[26:27], v[98:99]
	v_pk_fma_f32 v[104:105], v[24:25], v[32:33], v[102:103] neg_lo:[0,0,1] neg_hi:[0,0,1]
	v_pk_fma_f32 v[102:103], v[22:23], v[30:31], v[110:111] neg_lo:[0,0,1] neg_hi:[0,0,1]
	v_pk_mul_f32 v[24:25], v[24:25], v[100:101]
	v_pk_mul_f32 v[22:23], v[22:23], v[98:99]
	v_pk_fma_f32 v[28:29], v[28:29], v[32:33], v[24:25]
	v_pk_fma_f32 v[26:27], v[26:27], v[30:31], v[22:23]
	v_mov_b64_e32 v[30:31], v[106:107]
	v_mov_b64_e32 v[22:23], v[102:103]
	v_mov_b64_e32 v[32:33], v[108:109]
	v_mov_b64_e32 v[24:25], v[104:105]

; #define LAS __attribute__((address_space(3)))
; __device__ __forceinline__ unsigned cvt_pk_bf16(float lo, float hi) { unsigned r; asm volatile("v_cvt_pk_bf16_f32 %0, %1, %2" : "=v"(r) : "v"(lo), "v"(hi)); return r; }
;     __device__ __forceinline__ void operator()(const f32x4 (&acc)[2][2][4][2], const Unit& u, int wr, int wc, int fr, int fq) const {
;     ...
;                 if (!isv) {
;                     const f32x4 s4 = (acc[ai][0][m][0] * acc[ai][0][m][0] + acc[ai][0][m][1] * acc[ai][0][m][1]) + (acc[ai][1][m][0] * acc[ai][1][m][0] + acc[ai][1][m][1] * acc[ai][1][m][1]);
;                     float ss = (s4[0] + s4[1]) + (s4[2] + s4[3]);
;                     ss += __shfl_xor(ss, 16); ss += __shfl_xor(ss, 32);
;                     const float rs = __builtin_amdgcn_rsqf(ss * (1.0f / 64.0f) + EPSA) * qs;
; #pragma unroll
;                     for (int bj = 0; bj < 2; ++bj)
; #pragma unroll
;                         for (int n = 0; n < 2; ++n) v[bj][n] = acc[ai][bj][m][n] * (gv[bj][n] * rs);
;                     if (lat) {
; #pragma unroll
;                         for (int bj = 0; bj < 2; ++bj) { const int pos = bj ? (m * 16 + fr) : ((u.pm & 7) * 4 + ai * 2 + wr);
;                             const f32x4 cx = *(const LAS f32x4*)(ropeL + pos * 32 + 4 * fq), cy = *(const LAS f32x4*)(ropeL + pos * 32 + 16 + 4 * fq), a = v[bj][0], b = v[bj][1];
;                             v[bj][0] = a * cx - b * cy; v[bj][1] = a * cy + b * cx; }
;                     }
;                 } else {
; #pragma unroll
;                     for (int bj = 0; bj < 2; ++bj)
; #pragma unroll
;                         for (int n = 0; n < 2; ++n) v[bj][n] = acc[ai][bj][m][n] * ds;
;                 }
;                 bf16_t* dst;
;                 if (isq) dst = Q + (size_t)r * D + (grp * 8 + pl * 4 + wc) * HD;
;                 else if (!isv) dst = Kb + (size_t)kv_row(r) * KVP + (grp * 2 + wc) * HD;
;                 else dst = Vb + (size_t)kv_row(r) * KVP + (grp * 2 + wc - 2) * HD;
; #pragma unroll
;                 for (int bj = 0; bj < 2; ++bj)
; #pragma unroll
;                     for (int n = 0; n < 2; ++n) { u32x2 w; w.x = cvt_pk_bf16(v[bj][n][0], v[bj][n][1]); w.y = cvt_pk_bf16(v[bj][n][2], v[bj][n][3]);
;                         *(u32x2*)(dst + 32 * bj + 16 * n + 4 * fq) = w; }
.LBB0_738:
	v_lshl_add_u64 v[84:85], v[84:85], 0, v[190:191]
	v_cvt_pk_bf16_f32 v30, v30, v31
	v_cvt_pk_bf16_f32 v31, v32, v33
	global_store_dwordx2 v[84:85], v[30:31], off
	v_cvt_pk_bf16_f32 v18, v18, v19
	v_cvt_pk_bf16_f32 v19, v20, v21
	global_store_dwordx2 v[84:85], v[18:19], off offset:32
	v_cvt_pk_bf16_f32 v18, v22, v23
	v_cvt_pk_bf16_f32 v19, v24, v25
	global_store_dwordx2 v[84:85], v[18:19], off offset:64
	v_cvt_pk_bf16_f32 v18, v26, v27
	v_cvt_pk_bf16_f32 v19, v28, v29
	s_and_b64 vcc, exec, s[40:41]
	s_mov_b64 s[2:3], -1
	global_store_dwordx2 v[84:85], v[18:19], off offset:96
	s_cbranch_vccnz .LBB0_742
	v_pk_mul_f32 v[18:19], v[68:69], v[68:69]
	v_pk_mul_f32 v[20:21], v[66:67], v[66:67]
	v_pk_mul_f32 v[22:23], v[76:77], v[76:77]
	v_pk_mul_f32 v[24:25], v[74:75], v[74:75]
	v_pk_fma_f32 v[18:19], v[72:73], v[72:73], v[18:19]
	v_pk_fma_f32 v[20:21], v[70:71], v[70:71], v[20:21]
	v_pk_fma_f32 v[22:23], v[80:81], v[80:81], v[22:23]
	v_pk_fma_f32 v[24:25], v[78:79], v[78:79], v[24:25]
	v_pk_add_f32 v[18:19], v[18:19], v[22:23]
	v_pk_add_f32 v[20:21], v[20:21], v[24:25]
	s_nop 0
	v_pk_mov_b32 v[22:23], v[20:21], v[18:19] op_sel:[1,0]
	v_mov_b32_e32 v21, v19
	v_pk_add_f32 v[18:19], v[22:23], v[20:21]
	v_and_b32_e32 v20, 64, v211
	v_add_f32_e32 v18, v18, v19
	v_xor_b32_e32 v19, 16, v211
	v_add_u32_e32 v20, 64, v20
	v_cmp_lt_i32_e32 vcc, v19, v20
	s_nop 1
	v_cndmask_b32_e32 v19, v211, v19, vcc
	v_lshlrev_b32_e32 v19, 2, v19
	s_waitcnt lgkmcnt(0)
	v_mov_b32_e32 v19, v18
	s_nop 1
	v_permlane16_swap_b32_e32 v19, v18
	v_add_f32_e32 v18, v18, v19
	v_xor_b32_e32 v19, 32, v211
	v_cmp_lt_i32_e32 vcc, v19, v20
	s_nop 1
	v_cndmask_b32_e32 v19, v211, v19, vcc
	v_lshlrev_b32_e32 v19, 2, v19
	s_and_b64 vcc, exec, s[38:39]
	s_waitcnt lgkmcnt(0)
	v_mov_b32_e32 v19, v18
	s_nop 1
	v_permlane32_swap_b32_e32 v19, v18
	v_add_f32_e32 v18, v18, v19
	v_fmamk_f32 v18, v18, 0x3c800000, v210
	v_rsq_f32_e32 v18, v18
	s_nop 0
	v_mul_f32_e32 v26, v173, v18
	v_pk_mul_f32 v[18:19], v[14:15], v[26:27] op_sel_hi:[1,0]
	v_pk_mul_f32 v[20:21], v[16:17], v[26:27] op_sel_hi:[1,0]
	v_pk_mul_f32 v[30:31], v[70:71], v[18:19]
	v_pk_mul_f32 v[32:33], v[72:73], v[20:21]
	v_pk_mul_f32 v[18:19], v[10:11], v[26:27] op_sel_hi:[1,0]
	v_pk_mul_f32 v[20:21], v[12:13], v[26:27] op_sel_hi:[1,0]
	v_pk_mul_f32 v[22:23], v[6:7], v[26:27] op_sel_hi:[1,0]
	v_pk_mul_f32 v[24:25], v[8:9], v[26:27] op_sel_hi:[1,0]
	v_pk_mul_f32 v[84:85], v[2:3], v[26:27] op_sel_hi:[1,0]
	v_pk_mul_f32 v[26:27], v[4:5], v[26:27] op_sel_hi:[1,0]
	v_pk_mul_f32 v[20:21], v[68:69], v[20:21]
	v_pk_mul_f32 v[18:19], v[66:67], v[18:19]
	v_pk_mul_f32 v[24:25], v[80:81], v[24:25]
	v_pk_mul_f32 v[22:23], v[78:79], v[22:23]
	v_pk_mul_f32 v[28:29], v[76:77], v[26:27]
	v_pk_mul_f32 v[26:27], v[74:75], v[84:85]
	s_cbranch_vccnz .LBB0_741
	v_lshl_add_u32 v83, s30, 7, v170
	ds_read_b128 v[84:87], v83
	ds_read_b128 v[88:91], v83 offset:64
	s_waitcnt lgkmcnt(0)
	v_pk_mul_f32 v[92:93], v[20:21], v[90:91]
	v_pk_mul_f32 v[96:97], v[18:19], v[88:89]
	v_pk_fma_f32 v[94:95], v[32:33], v[86:87], v[92:93] neg_lo:[0,0,1] neg_hi:[0,0,1]
	v_pk_fma_f32 v[92:93], v[30:31], v[84:85], v[96:97] neg_lo:[0,0,1] neg_hi:[0,0,1]
	v_pk_mul_f32 v[32:33], v[32:33], v[90:91]
	v_pk_mul_f32 v[30:31], v[30:31], v[88:89]
	v_pk_fma_f32 v[20:21], v[20:21], v[86:87], v[32:33]
	v_pk_fma_f32 v[18:19], v[18:19], v[84:85], v[30:31]
	ds_read_b128 v[30:33], v171 offset:2048
	ds_read_b128 v[84:87], v171 offset:2112
	s_waitcnt lgkmcnt(0)
	v_pk_mul_f32 v[88:89], v[28:29], v[86:87]
	v_pk_mul_f32 v[96:97], v[26:27], v[84:85]
	v_pk_fma_f32 v[90:91], v[24:25], v[32:33], v[88:89] neg_lo:[0,0,1] neg_hi:[0,0,1]
	v_pk_fma_f32 v[88:89], v[22:23], v[30:31], v[96:97] neg_lo:[0,0,1] neg_hi:[0,0,1]
	v_pk_mul_f32 v[24:25], v[24:25], v[86:87]
	v_pk_mul_f32 v[22:23], v[22:23], v[84:85]
	v_pk_fma_f32 v[28:29], v[28:29], v[32:33], v[24:25]
	v_pk_fma_f32 v[26:27], v[26:27], v[30:31], v[22:23]
	v_mov_b64_e32 v[30:31], v[92:93]
	v_mov_b64_e32 v[22:23], v[88:89]
	v_mov_b64_e32 v[32:33], v[94:95]
	v_mov_b64_e32 v[24:25], v[90:91]

; #define LAS __attribute__((address_space(3)))
; __device__ __forceinline__ unsigned cvt_pk_bf16(float lo, float hi) { unsigned r; asm volatile("v_cvt_pk_bf16_f32 %0, %1, %2" : "=v"(r) : "v"(lo), "v"(hi)); return r; }
;     __device__ __forceinline__ void operator()(const f32x4 (&acc)[2][2][4][2], const Unit& u, int wr, int wc, int fr, int fq) const {
;     ...
;                 if (!isv) {
;                     const f32x4 s4 = (acc[ai][0][m][0] * acc[ai][0][m][0] + acc[ai][0][m][1] * acc[ai][0][m][1]) + (acc[ai][1][m][0] * acc[ai][1][m][0] + acc[ai][1][m][1] * acc[ai][1][m][1]);
;                     float ss = (s4[0] + s4[1]) + (s4[2] + s4[3]);
;                     ss += __shfl_xor(ss, 16); ss += __shfl_xor(ss, 32);
;                     const float rs = __builtin_amdgcn_rsqf(ss * (1.0f / 64.0f) + EPSA) * qs;
; #pragma unroll
;                     for (int bj = 0; bj < 2; ++bj)
; #pragma unroll
;                         for (int n = 0; n < 2; ++n) v[bj][n] = acc[ai][bj][m][n] * (gv[bj][n] * rs);
;                     if (lat) {
; #pragma unroll
;                         for (int bj = 0; bj < 2; ++bj) { const int pos = bj ? (m * 16 + fr) : ((u.pm & 7) * 4 + ai * 2 + wr);
;                             const f32x4 cx = *(const LAS f32x4*)(ropeL + pos * 32 + 4 * fq), cy = *(const LAS f32x4*)(ropeL + pos * 32 + 16 + 4 * fq), a = v[bj][0], b = v[bj][1];
;                             v[bj][0] = a * cx - b * cy; v[bj][1] = a * cy + b * cx; }
;                     }
;                 } else {
; #pragma unroll
;                     for (int bj = 0; bj < 2; ++bj)
; #pragma unroll
;                         for (int n = 0; n < 2; ++n) v[bj][n] = acc[ai][bj][m][n] * ds;
;                 }
;                 bf16_t* dst;
;                 if (isq) dst = Q + (size_t)r * D + (grp * 8 + pl * 4 + wc) * HD;
;                 else if (!isv) dst = Kb + (size_t)kv_row(r) * KVP + (grp * 2 + wc) * HD;
;                 else dst = Vb + (size_t)kv_row(r) * KVP + (grp * 2 + wc - 2) * HD;
; #pragma unroll
;                 for (int bj = 0; bj < 2; ++bj)
; #pragma unroll
;                     for (int n = 0; n < 2; ++n) { u32x2 w; w.x = cvt_pk_bf16(v[bj][n][0], v[bj][n][1]); w.y = cvt_pk_bf16(v[bj][n][2], v[bj][n][3]);
;                         *(u32x2*)(dst + 32 * bj + 16 * n + 4 * fq) = w; }
.LBB0_751:
	v_lshl_add_u64 v[66:67], v[66:67], 0, v[190:191]
	v_cvt_pk_bf16_f32 v30, v30, v31
	v_cvt_pk_bf16_f32 v31, v32, v33
	global_store_dwordx2 v[66:67], v[30:31], off
	v_cvt_pk_bf16_f32 v18, v18, v19
	v_cvt_pk_bf16_f32 v19, v20, v21
	global_store_dwordx2 v[66:67], v[18:19], off offset:32
	v_cvt_pk_bf16_f32 v18, v22, v23
	v_cvt_pk_bf16_f32 v19, v24, v25
	global_store_dwordx2 v[66:67], v[18:19], off offset:64
	v_cvt_pk_bf16_f32 v18, v26, v27
	v_cvt_pk_bf16_f32 v19, v28, v29
	s_and_b64 vcc, exec, s[40:41]
	s_mov_b64 s[2:3], -1
	global_store_dwordx2 v[66:67], v[18:19], off offset:96
	s_cbranch_vccnz .LBB0_755
	v_pk_mul_f32 v[18:19], v[52:53], v[52:53]
	v_pk_mul_f32 v[20:21], v[50:51], v[50:51]
	v_pk_mul_f32 v[22:23], v[56:57], v[56:57]
	v_pk_mul_f32 v[24:25], v[54:55], v[54:55]
	v_pk_fma_f32 v[18:19], v[60:61], v[60:61], v[18:19]
	v_pk_fma_f32 v[20:21], v[58:59], v[58:59], v[20:21]
	v_pk_fma_f32 v[22:23], v[64:65], v[64:65], v[22:23]
	v_pk_fma_f32 v[24:25], v[62:63], v[62:63], v[24:25]
	v_pk_add_f32 v[18:19], v[18:19], v[22:23]
	v_pk_add_f32 v[20:21], v[20:21], v[24:25]
	s_nop 0
	v_pk_mov_b32 v[22:23], v[20:21], v[18:19] op_sel:[1,0]
	v_mov_b32_e32 v21, v19
	v_pk_add_f32 v[18:19], v[22:23], v[20:21]
	v_and_b32_e32 v20, 64, v211
	v_add_f32_e32 v18, v18, v19
	v_xor_b32_e32 v19, 16, v211
	v_add_u32_e32 v20, 64, v20
	v_cmp_lt_i32_e32 vcc, v19, v20
	s_nop 1
	v_cndmask_b32_e32 v19, v211, v19, vcc
	v_lshlrev_b32_e32 v19, 2, v19
	s_waitcnt lgkmcnt(0)
	v_mov_b32_e32 v19, v18
	s_nop 1
	v_permlane16_swap_b32_e32 v19, v18
	v_add_f32_e32 v18, v18, v19
	v_xor_b32_e32 v19, 32, v211
	v_cmp_lt_i32_e32 vcc, v19, v20
	s_nop 1
	v_cndmask_b32_e32 v19, v211, v19, vcc
	v_lshlrev_b32_e32 v19, 2, v19
	s_and_b64 vcc, exec, s[38:39]
	s_waitcnt lgkmcnt(0)
	v_mov_b32_e32 v19, v18
	s_nop 1
	v_permlane32_swap_b32_e32 v19, v18
	v_add_f32_e32 v18, v18, v19
	v_fmamk_f32 v18, v18, 0x3c800000, v210
	v_rsq_f32_e32 v18, v18
	s_nop 0
	v_mul_f32_e32 v26, v173, v18
	v_pk_mul_f32 v[18:19], v[14:15], v[26:27] op_sel_hi:[1,0]
	v_pk_mul_f32 v[20:21], v[16:17], v[26:27] op_sel_hi:[1,0]
	v_pk_mul_f32 v[30:31], v[58:59], v[18:19]
	v_pk_mul_f32 v[32:33], v[60:61], v[20:21]
	v_pk_mul_f32 v[18:19], v[10:11], v[26:27] op_sel_hi:[1,0]
	v_pk_mul_f32 v[20:21], v[12:13], v[26:27] op_sel_hi:[1,0]
	v_pk_mul_f32 v[22:23], v[6:7], v[26:27] op_sel_hi:[1,0]
	v_pk_mul_f32 v[24:25], v[8:9], v[26:27] op_sel_hi:[1,0]
	v_pk_mul_f32 v[66:67], v[2:3], v[26:27] op_sel_hi:[1,0]
	v_pk_mul_f32 v[26:27], v[4:5], v[26:27] op_sel_hi:[1,0]
	v_pk_mul_f32 v[20:21], v[52:53], v[20:21]
	v_pk_mul_f32 v[18:19], v[50:51], v[18:19]
	v_pk_mul_f32 v[24:25], v[64:65], v[24:25]
	v_pk_mul_f32 v[22:23], v[62:63], v[22:23]
	v_pk_mul_f32 v[28:29], v[56:57], v[26:27]
	v_pk_mul_f32 v[26:27], v[54:55], v[66:67]
	s_cbranch_vccnz .LBB0_754
	v_lshl_add_u32 v70, s30, 7, v170
	ds_read_b128 v[66:69], v70
	ds_read_b128 v[70:73], v70 offset:64
	s_waitcnt lgkmcnt(0)
	v_pk_mul_f32 v[74:75], v[20:21], v[72:73]
	v_pk_mul_f32 v[78:79], v[18:19], v[70:71]
	v_pk_fma_f32 v[76:77], v[32:33], v[68:69], v[74:75] neg_lo:[0,0,1] neg_hi:[0,0,1]
	v_pk_fma_f32 v[74:75], v[30:31], v[66:67], v[78:79] neg_lo:[0,0,1] neg_hi:[0,0,1]
	v_pk_mul_f32 v[32:33], v[32:33], v[72:73]
	v_pk_mul_f32 v[30:31], v[30:31], v[70:71]
	v_pk_fma_f32 v[20:21], v[20:21], v[68:69], v[32:33]
	v_pk_fma_f32 v[18:19], v[18:19], v[66:67], v[30:31]
	ds_read_b128 v[30:33], v171 offset:4096
	ds_read_b128 v[66:69], v171 offset:4160
	s_waitcnt lgkmcnt(0)
	v_pk_mul_f32 v[70:71], v[28:29], v[68:69]
	v_pk_mul_f32 v[78:79], v[26:27], v[66:67]
	v_pk_fma_f32 v[72:73], v[24:25], v[32:33], v[70:71] neg_lo:[0,0,1] neg_hi:[0,0,1]
	v_pk_fma_f32 v[70:71], v[22:23], v[30:31], v[78:79] neg_lo:[0,0,1] neg_hi:[0,0,1]
	v_pk_mul_f32 v[24:25], v[24:25], v[68:69]
	v_pk_mul_f32 v[22:23], v[22:23], v[66:67]
	v_pk_fma_f32 v[28:29], v[28:29], v[32:33], v[24:25]
	v_pk_fma_f32 v[26:27], v[26:27], v[30:31], v[22:23]
	v_mov_b64_e32 v[30:31], v[74:75]
	v_mov_b64_e32 v[22:23], v[70:71]
	v_mov_b64_e32 v[32:33], v[76:77]
	v_mov_b64_e32 v[24:25], v[72:73]

; #define LAS __attribute__((address_space(3)))
; __device__ __forceinline__ unsigned cvt_pk_bf16(float lo, float hi) { unsigned r; asm volatile("v_cvt_pk_bf16_f32 %0, %1, %2" : "=v"(r) : "v"(lo), "v"(hi)); return r; }
;     __device__ __forceinline__ void operator()(const f32x4 (&acc)[2][2][4][2], const Unit& u, int wr, int wc, int fr, int fq) const {
;     ...
;                 if (!isv) {
;                     const f32x4 s4 = (acc[ai][0][m][0] * acc[ai][0][m][0] + acc[ai][0][m][1] * acc[ai][0][m][1]) + (acc[ai][1][m][0] * acc[ai][1][m][0] + acc[ai][1][m][1] * acc[ai][1][m][1]);
;                     float ss = (s4[0] + s4[1]) + (s4[2] + s4[3]);
;                     ss += __shfl_xor(ss, 16); ss += __shfl_xor(ss, 32);
;                     const float rs = __builtin_amdgcn_rsqf(ss * (1.0f / 64.0f) + EPSA) * qs;
; #pragma unroll
;                     for (int bj = 0; bj < 2; ++bj)
; #pragma unroll
;                         for (int n = 0; n < 2; ++n) v[bj][n] = acc[ai][bj][m][n] * (gv[bj][n] * rs);
;                     if (lat) {
; #pragma unroll
;                         for (int bj = 0; bj < 2; ++bj) { const int pos = bj ? (m * 16 + fr) : ((u.pm & 7) * 4 + ai * 2 + wr);
;                             const f32x4 cx = *(const LAS f32x4*)(ropeL + pos * 32 + 4 * fq), cy = *(const LAS f32x4*)(ropeL + pos * 32 + 16 + 4 * fq), a = v[bj][0], b = v[bj][1];
;                             v[bj][0] = a * cx - b * cy; v[bj][1] = a * cy + b * cx; }
;                     }
;                 } else {
; #pragma unroll
;                     for (int bj = 0; bj < 2; ++bj)
; #pragma unroll
;                         for (int n = 0; n < 2; ++n) v[bj][n] = acc[ai][bj][m][n] * ds;
;                 }
;                 bf16_t* dst;
;                 if (isq) dst = Q + (size_t)r * D + (grp * 8 + pl * 4 + wc) * HD;
;                 else if (!isv) dst = Kb + (size_t)kv_row(r) * KVP + (grp * 2 + wc) * HD;
;                 else dst = Vb + (size_t)kv_row(r) * KVP + (grp * 2 + wc - 2) * HD;
; #pragma unroll
;                 for (int bj = 0; bj < 2; ++bj)
; #pragma unroll
;                     for (int n = 0; n < 2; ++n) { u32x2 w; w.x = cvt_pk_bf16(v[bj][n][0], v[bj][n][1]); w.y = cvt_pk_bf16(v[bj][n][2], v[bj][n][3]);
;                         *(u32x2*)(dst + 32 * bj + 16 * n + 4 * fq) = w; }
.LBB0_764:
	v_lshl_add_u64 v[50:51], v[50:51], 0, v[190:191]
	v_cvt_pk_bf16_f32 v30, v30, v31
	v_cvt_pk_bf16_f32 v31, v32, v33
	global_store_dwordx2 v[50:51], v[30:31], off
	v_cvt_pk_bf16_f32 v18, v18, v19
	v_cvt_pk_bf16_f32 v19, v20, v21
	global_store_dwordx2 v[50:51], v[18:19], off offset:32
	v_cvt_pk_bf16_f32 v18, v22, v23
	v_cvt_pk_bf16_f32 v19, v24, v25
	global_store_dwordx2 v[50:51], v[18:19], off offset:64
	v_cvt_pk_bf16_f32 v18, v26, v27
	v_cvt_pk_bf16_f32 v19, v28, v29
	s_and_b64 vcc, exec, s[40:41]
	s_mov_b64 s[2:3], -1
	global_store_dwordx2 v[50:51], v[18:19], off offset:96
	s_cbranch_vccnz .LBB0_768
	v_pk_mul_f32 v[18:19], v[40:41], v[40:41]
	v_pk_mul_f32 v[20:21], v[38:39], v[38:39]
	v_pk_mul_f32 v[22:23], v[36:37], v[36:37]
	v_pk_mul_f32 v[24:25], v[34:35], v[34:35]
	v_pk_fma_f32 v[18:19], v[48:49], v[48:49], v[18:19]
	v_pk_fma_f32 v[20:21], v[46:47], v[46:47], v[20:21]
	v_pk_fma_f32 v[22:23], v[44:45], v[44:45], v[22:23]
	v_pk_fma_f32 v[24:25], v[42:43], v[42:43], v[24:25]
	v_pk_add_f32 v[18:19], v[18:19], v[22:23]
	v_pk_add_f32 v[20:21], v[20:21], v[24:25]
	s_nop 0
	v_pk_mov_b32 v[22:23], v[20:21], v[18:19] op_sel:[1,0]
	v_mov_b32_e32 v21, v19
	v_pk_add_f32 v[18:19], v[22:23], v[20:21]
	v_and_b32_e32 v20, 64, v211
	v_add_f32_e32 v18, v18, v19
	v_xor_b32_e32 v19, 16, v211
	v_add_u32_e32 v20, 64, v20
	v_cmp_lt_i32_e32 vcc, v19, v20
	s_nop 1
	v_cndmask_b32_e32 v19, v211, v19, vcc
	v_lshlrev_b32_e32 v19, 2, v19
	s_waitcnt lgkmcnt(0)
	v_mov_b32_e32 v19, v18
	s_nop 1
	v_permlane16_swap_b32_e32 v19, v18
	v_add_f32_e32 v18, v18, v19
	v_xor_b32_e32 v19, 32, v211
	v_cmp_lt_i32_e32 vcc, v19, v20
	s_nop 1
	v_cndmask_b32_e32 v19, v211, v19, vcc
	v_lshlrev_b32_e32 v19, 2, v19
	s_and_b64 vcc, exec, s[38:39]
	s_waitcnt lgkmcnt(0)
	v_mov_b32_e32 v19, v18
	s_nop 1
	v_permlane32_swap_b32_e32 v19, v18
	v_add_f32_e32 v18, v18, v19
	v_fmamk_f32 v18, v18, 0x3c800000, v210
	v_rsq_f32_e32 v18, v18
	s_nop 0
	v_mul_f32_e32 v26, v173, v18
	v_pk_mul_f32 v[14:15], v[14:15], v[26:27] op_sel_hi:[1,0]
	v_pk_mul_f32 v[16:17], v[16:17], v[26:27] op_sel_hi:[1,0]
	v_pk_mul_f32 v[10:11], v[10:11], v[26:27] op_sel_hi:[1,0]
	v_pk_mul_f32 v[12:13], v[12:13], v[26:27] op_sel_hi:[1,0]
	v_pk_mul_f32 v[6:7], v[6:7], v[26:27] op_sel_hi:[1,0]
	v_pk_mul_f32 v[8:9], v[8:9], v[26:27] op_sel_hi:[1,0]
	v_pk_mul_f32 v[2:3], v[2:3], v[26:27] op_sel_hi:[1,0]
	v_pk_mul_f32 v[4:5], v[4:5], v[26:27] op_sel_hi:[1,0]
	v_pk_mul_f32 v[32:33], v[48:49], v[16:17]
	v_pk_mul_f32 v[30:31], v[46:47], v[14:15]
	v_pk_mul_f32 v[20:21], v[40:41], v[12:13]
	v_pk_mul_f32 v[18:19], v[38:39], v[10:11]
	v_pk_mul_f32 v[24:25], v[44:45], v[8:9]
	v_pk_mul_f32 v[22:23], v[42:43], v[6:7]
	v_pk_mul_f32 v[28:29], v[36:37], v[4:5]
	v_pk_mul_f32 v[26:27], v[34:35], v[2:3]
	s_cbranch_vccnz .LBB0_767
	v_lshl_add_u32 v6, s30, 7, v170
	ds_read_b128 v[2:5], v6
	ds_read_b128 v[6:9], v6 offset:64
	s_waitcnt lgkmcnt(0)
	v_pk_mul_f32 v[10:11], v[20:21], v[8:9]
	v_pk_mul_f32 v[14:15], v[18:19], v[6:7]
	v_pk_mul_f32 v[8:9], v[32:33], v[8:9]
	v_pk_mul_f32 v[6:7], v[30:31], v[6:7]
	v_pk_fma_f32 v[12:13], v[32:33], v[4:5], v[10:11] neg_lo:[0,0,1] neg_hi:[0,0,1]
	v_pk_fma_f32 v[10:11], v[30:31], v[2:3], v[14:15] neg_lo:[0,0,1] neg_hi:[0,0,1]
	v_pk_fma_f32 v[20:21], v[20:21], v[4:5], v[8:9]
	v_pk_fma_f32 v[18:19], v[18:19], v[2:3], v[6:7]
	ds_read_b128 v[2:5], v171 offset:6144
	ds_read_b128 v[6:9], v171 offset:6208
	s_waitcnt lgkmcnt(0)
	v_pk_mul_f32 v[14:15], v[28:29], v[8:9]
	v_pk_mul_f32 v[30:31], v[26:27], v[6:7]
	v_pk_fma_f32 v[16:17], v[24:25], v[4:5], v[14:15] neg_lo:[0,0,1] neg_hi:[0,0,1]
	v_pk_fma_f32 v[14:15], v[22:23], v[2:3], v[30:31] neg_lo:[0,0,1] neg_hi:[0,0,1]
	v_pk_mul_f32 v[8:9], v[24:25], v[8:9]
	v_pk_mul_f32 v[6:7], v[22:23], v[6:7]
	v_mov_b64_e32 v[32:33], v[12:13]
	v_mov_b64_e32 v[24:25], v[16:17]
	v_pk_fma_f32 v[28:29], v[28:29], v[4:5], v[8:9]
	v_pk_fma_f32 v[26:27], v[26:27], v[2:3], v[6:7]
	v_mov_b64_e32 v[30:31], v[10:11]
	v_mov_b64_e32 v[22:23], v[14:15]
